# speedup vs baseline: 1.0073x; 1.0023x over previous
_Z11attn_kernelPKDF16_PDF16_PKfS3_S3_PfS4_ii:
	s_load_dwordx2 s[12:13], s[0:1], 0x0
	s_cmpk_lt_u32 s2, 0x200
	s_mov_b64 s[4:5], -1
	s_cbranch_scc0 .LBB2_36
	v_lshrrev_b32_e32 v92, 6, v0
	s_movk_i32 s3, 0x100
	v_cmp_gt_u32_e64 s[6:7], s3, v0
	s_movk_i32 s3, 0xff
	v_lshlrev_b32_e32 v2, 4, v92
	v_lshlrev_b32_e32 v108, 3, v0
	v_cmp_lt_u32_e32 vcc, s3, v0
	v_and_b32_e32 v1, 32, v2
	v_and_b32_e32 v18, 24, v108
	s_movk_i32 s3, 0x400
	v_bfe_u32 v3, v0, 2, 4
	v_or3_b32 v4, v1, v18, s3
	s_and_saveexec_b64 s[4:5], vcc
	s_xor_b64 s[4:5], exec, s[4:5]
	v_lshlrev_b32_e32 v1, 5, v92
	v_and_or_b32 v1, v1, 32, v3
	s_movk_i32 s3, 0x640
	v_mad_u32_u24 v82, v1, s3, v4
	s_or_saveexec_b64 s[4:5], s[4:5]
	v_bfe_u32 v109, v0, 3, 3
	s_xor_b64 exec, exec, s[4:5]
	v_or_b32_e32 v1, v2, v109
	v_lshrrev_b32_e32 v2, 1, v1
	v_xor_b32_e32 v2, v2, v0
	v_mul_u32_u24_e32 v1, 0x640, v1
	v_lshlrev_b32_e32 v2, 3, v2
	v_and_or_b32 v1, v2, 56, v1
	v_add_u32_e32 v82, 0x200, v1
	s_or_b64 exec, exec, s[4:5]
	v_and_b32_e32 v96, 3, v92
	v_lshl_or_b32 v5, v96, 1, 1
	s_and_saveexec_b64 s[4:5], vcc
	s_xor_b64 s[4:5], exec, s[4:5]
	v_lshlrev_b32_e32 v1, 4, v5
	v_and_or_b32 v1, v1, 48, v3
	s_movk_i32 s3, 0x640
	v_mad_u32_u24 v2, v1, s3, v4
	s_or_saveexec_b64 s[4:5], s[4:5]
	v_and_b32_e32 v94, 63, v0
	s_xor_b64 exec, exec, s[4:5]
	v_lshl_or_b32 v1, v5, 3, v109
	v_lshrrev_b32_e32 v2, 1, v1
	v_xor_b32_e32 v2, v2, v0
	v_mul_u32_u24_e32 v1, 0x640, v1
	v_lshlrev_b32_e32 v2, 3, v2
	v_and_or_b32 v1, v2, 56, v1
	v_add_u32_e32 v2, 0x200, v1
	s_or_b64 exec, exec, s[4:5]
	v_mov_b32_e32 v1, 0x100
	v_sub_co_u32_e32 v1, vcc, s2, v1
	s_lshr_b32 s3, s2, 6
	v_readfirstlane_b32 s4, v1
	s_sub_i32 s3, 7, s3
	s_lshr_b32 s8, s4, 6
	s_and_b64 s[4:5], vcc, exec
	s_cselect_b32 s4, s3, s8
	v_and_b32_e32 v95, 31, v0
	s_lshl_b32 s18, s4, 7
	s_lshl_b32 s3, s2, 10
	v_lshlrev_b32_e32 v110, 5, v96
	s_and_b32 s19, s3, 0x1c00
	v_or3_b32 v99, v110, v95, s18
	s_lshl_b32 s3, s2, 3
	v_add_u32_e32 v3, s19, v99
	s_and_b32 s3, s3, 0x1c0
	s_lshl_b32 s21, s4, 1
	s_movk_i32 s4, 0xc80
	s_waitcnt lgkmcnt(0)
	v_mov_b64_e32 v[4:5], s[12:13]
	s_mov_b32 s5, 0
	v_mad_u64_u32 v[4:5], s[8:9], v3, s4, v[4:5]
	s_lshl_b32 s4, s3, 1
	s_mul_i32 s14, s19, 0xc80
	v_lshl_add_u64 v[4:5], v[4:5], 0, s[4:5]
	s_add_u32 s5, s12, s14
	s_addc_u32 s8, s13, 0
	s_add_u32 s4, s5, s4
	s_addc_u32 s5, s8, 0
	v_lshlrev_b32_e32 v34, 11, v92
	s_cmp_lg_u32 0, -1
	v_mov_b32_e32 v83, 0
	v_readfirstlane_b32 s8, v34
	s_cselect_b32 s9, 0, 0
	v_lshlrev_b64 v[84:85], 1, v[82:83]
	s_add_i32 s8, s8, s9
	v_lshl_add_u64 v[6:7], s[4:5], 0, v[84:85]
	s_mov_b32 s9, m0
	s_mov_b32 m0, s8
	s_nop 0
	global_load_lds_dwordx4 v[6:7], off
	s_mov_b32 m0, s9
	v_mov_b32_e32 v3, v83
	v_lshlrev_b64 v[86:87], 1, v[2:3]
	s_add_i32 s9, s8, 0x400
	v_lshl_add_u64 v[2:3], s[4:5], 0, v[86:87]
	s_mov_b32 s10, m0
	s_mov_b32 m0, s9
	s_nop 0
	global_load_lds_dwordx4 v[2:3], off
	s_mov_b32 m0, s10
	s_add_i32 s9, s8, 0x4000
	s_add_u32 s4, s4, 0x32000
	s_addc_u32 s5, s5, 0
	v_lshrrev_b32_e32 v93, 5, v94
	v_lshl_add_u64 v[2:3], s[4:5], 0, v[84:85]
	s_mov_b32 s10, m0
	s_mov_b32 m0, s9
	s_nop 0
	global_load_lds_dwordx4 v[2:3], off
	s_mov_b32 m0, s10
	v_lshl_add_u64 v[2:3], s[4:5], 0, v[86:87]
	v_lshlrev_b32_e32 v82, 4, v93
	s_addk_i32 s8, 0x4400
	s_mov_b32 s4, m0
	s_mov_b32 m0, s8
	s_nop 0
	global_load_lds_dwordx4 v[2:3], off
	s_mov_b32 m0, s4
	v_lshl_add_u64 v[2:3], v[4:5], 0, v[82:83]
	global_load_dwordx4 v[78:81], v[2:3], off
	global_load_dwordx4 v[74:77], v[2:3], off offset:32
	global_load_dwordx4 v[70:73], v[2:3], off offset:64
	global_load_dwordx4 v[66:69], v[2:3], off offset:96
	s_load_dwordx2 s[8:9], s[0:1], 0x8
	v_lshrrev_b32_e32 v2, 1, v0
	v_bfe_u32 v3, v0, 1, 3
	v_lshlrev_b32_e32 v4, 4, v0
	v_lshlrev_b32_e32 v5, 1, v0
	v_lshlrev_b32_e32 v19, 7, v95
	v_bitop3_b32 v20, v93, v2, 7 bitop3:0x78
	v_bitop3_b32 v21, v93, v3, 2 bitop3:0x36
	v_bitop3_b32 v22, v93, v3, 4 bitop3:0x36
	v_bitop3_b32 v23, v93, v3, 6 bitop3:0x36
	v_and_b32_e32 v24, 0xc0, v4
	v_and_b32_e32 v25, 32, v5
	v_mov_b32_e32 v16, v83
	v_mov_b32_e32 v17, v83
	v_lshl_or_b32 v106, v20, 4, v19
	v_lshl_or_b32 v105, v21, 4, v19
	v_lshl_or_b32 v104, v22, 4, v19
	v_lshl_or_b32 v103, v23, 4, v19
	v_lshl_or_b32 v19, v93, 8, v24
	v_lshrrev_b32_e32 v97, 8, v0
	v_mov_b32_e32 v2, v83
	v_mov_b32_e32 v3, v83
	v_mov_b32_e32 v4, v83
	v_mov_b32_e32 v5, v83
	v_mov_b32_e32 v6, v83
	v_mov_b32_e32 v7, v83
	v_mov_b32_e32 v8, v83
	v_mov_b32_e32 v9, v83
	v_mov_b32_e32 v10, v83
	v_mov_b32_e32 v11, v83
	v_mov_b32_e32 v12, v83
	v_mov_b32_e32 v13, v83
	v_mov_b32_e32 v14, v83
	v_mov_b32_e32 v15, v83
	v_or3_b32 v98, v19, v25, v18
	s_add_i32 s20, 0, 0x10000
	v_mov_b64_e32 v[32:33], v[16:17]
	v_cmp_gt_u32_e32 vcc, s21, v97
	v_lshl_add_u32 v100, v92, 7, s20
	v_mov_b32_e32 v102, 0xff800000
	v_mbcnt_lo_u32_b32 v101, -1, 0
	v_mov_b32_e32 v107, v97
	v_mov_b64_e32 v[30:31], v[14:15]
	v_mov_b64_e32 v[28:29], v[12:13]
	v_mov_b64_e32 v[26:27], v[10:11]
	v_mov_b64_e32 v[24:25], v[8:9]
	v_mov_b64_e32 v[22:23], v[6:7]
	v_mov_b64_e32 v[20:21], v[4:5]
	v_mov_b64_e32 v[18:19], v[2:3]
	s_waitcnt vmcnt(3)
	s_waitcnt vmcnt(2)
	s_waitcnt vmcnt(1)
	s_waitcnt vmcnt(0)
	s_and_saveexec_b64 s[10:11], vcc
	s_cbranch_execz .LBB2_18
	s_cmp_lg_u32 0, -1
	s_cselect_b32 s4, 0, 0
	s_lshl_b32 s15, s2, 4
	s_and_b32 s15, s15, 0x380
	s_add_u32 s14, s14, s15
	s_addc_u32 s15, 0, 0
	s_add_u32 s12, s12, s14
	v_mov_b32_e32 v2, 0
	s_addc_u32 s13, s13, s15
	v_mov_b32_e32 v16, v2
	v_mov_b32_e32 v17, v2
	s_add_u32 s12, s12, 0x96000
	v_mov_b32_e32 v3, v2
	v_mov_b32_e32 v4, v2
	v_mov_b32_e32 v5, v2
	v_mov_b32_e32 v6, v2
	v_mov_b32_e32 v7, v2
	v_mov_b32_e32 v8, v2
	v_mov_b32_e32 v9, v2
	v_mov_b32_e32 v10, v2
	v_mov_b32_e32 v11, v2
	v_mov_b32_e32 v12, v2
	v_mov_b32_e32 v13, v2
	v_mov_b32_e32 v14, v2
	v_mov_b32_e32 v15, v2
	v_mov_b64_e32 v[32:33], v[16:17]
	v_add_u32_e32 v108, s4, v34
	v_cmp_gt_u32_e64 s[4:5], 32, v94
	s_addc_u32 s13, s13, 0
	v_lshlrev_b32_e32 v109, 14, v97
	v_mov_b32_e32 v88, 0xff800000
	s_mov_b32 s22, 0xc000
	s_mov_b64 s[14:15], 0
	v_mbcnt_hi_u32_b32 v110, -1, v101
	s_mov_b32 s23, 0x3e38aa3b
	s_mov_b32 s24, 0x41000000
	v_add_u32_e32 v111, v100, v82
	s_mov_b32 s25, 0xff800000
	v_bfrev_b32_e32 v112, 1
	v_mov_b32_e32 v107, v97
	v_mov_b64_e32 v[30:31], v[14:15]
	v_mov_b64_e32 v[28:29], v[12:13]
	v_mov_b64_e32 v[26:27], v[10:11]
	v_mov_b64_e32 v[24:25], v[8:9]
	v_mov_b64_e32 v[22:23], v[6:7]
	v_mov_b64_e32 v[20:21], v[4:5]
	v_mov_b64_e32 v[18:19], v[2:3]
	v_mov_b32_e32 v113, v2
	s_branch .LBB2_13
